# baseline (speedup 1.0000x reference)
_Z16sum_layer_kernelPKfS0_Pf:
	s_load_dwordx4 s[4:7], s[0:1], 0x0
	s_load_dwordx2 s[8:9], s[0:1], 0x10
	v_and_b32_e32 v40, 31, v0
	v_bfe_u32 v41, v0, 5, 1
	v_lshrrev_b32_e32 v42, 6, v0
	v_and_b32_e32 v43, 7, v0
	v_bfe_u32 v44, v0, 3, 3
	v_and_b32_e32 v45, 63, v0
	s_lshl_b32 s3, s2, 12
	s_lshl_b32 s19, s2, 7
	v_lshlrev_b32_e32 v1, 11, v41
	v_lshl_or_b32 v1, v40, 2, v1
	v_lshlrev_b32_e32 v46, 4, v43
	v_lshl_add_u32 v35, v44, 16, v46
	v_lshl_add_u32 v35, v42, 21, v35
	v_add_u32_e32 v35, s19, v35
	v_lshlrev_b32_e32 v36, 4, v41
	v_lshl_add_u32 v36, v40, 16, v36
	v_lshl_add_u32 v36, v42, 21, v36
	v_add_u32_e32 v36, s19, v36
	v_mul_u32_u24_e32 v37, 0x1200, v42
	v_mul_u32_u24_e32 v38, 0x90, v44
	v_add3_u32 v38, v37, v38, v46
	v_mul_u32_u24_e32 v39, 0x90, v40
	v_lshlrev_b32_e32 v47, 6, v41
	v_add3_u32 v39, v37, v39, v47
	v_cmp_gt_u32_e32 vcc, 32, v45
	v_mov_b32_e32 v48, 0xc1600000
	s_mov_b32 s16, 0x3fb8aa3b
	s_mov_b32 s17, 0x3f317218
	s_mov_b32 s20, 0x80000
	s_mov_b32 s21, 0x100000
	s_mov_b32 s22, 0x180000
	s_mov_b32 s14, 0x200000
	s_mov_b32 s15, 0x20000
	s_waitcnt lgkmcnt(0)
	s_mov_b32 s12, s6
	s_and_b32 s13, s7, 0xffff
	s_and_b32 s5, s5, 0xffff
	s_mov_b32 s6, 0x800000
	s_mov_b32 s7, s15
	buffer_load_dword v18, v1, s[12:15], s3 offen nt
	buffer_load_dword v19, v1, s[12:15], s3 offen offset:128 nt
	buffer_load_dword v20, v1, s[12:15], s3 offen offset:256 nt
	buffer_load_dword v21, v1, s[12:15], s3 offen offset:384 nt
	buffer_load_dword v22, v1, s[12:15], s3 offen offset:512 nt
	buffer_load_dword v23, v1, s[12:15], s3 offen offset:640 nt
	buffer_load_dword v24, v1, s[12:15], s3 offen offset:768 nt
	buffer_load_dword v25, v1, s[12:15], s3 offen offset:896 nt
	buffer_load_dword v26, v1, s[12:15], s3 offen offset:1024 nt
	buffer_load_dword v27, v1, s[12:15], s3 offen offset:1152 nt
	buffer_load_dword v28, v1, s[12:15], s3 offen offset:1280 nt
	buffer_load_dword v29, v1, s[12:15], s3 offen offset:1408 nt
	buffer_load_dword v30, v1, s[12:15], s3 offen offset:1536 nt
	buffer_load_dword v31, v1, s[12:15], s3 offen offset:1664 nt
	buffer_load_dword v32, v1, s[12:15], s3 offen offset:1792 nt
	buffer_load_dword v33, v1, s[12:15], s3 offen offset:1920 nt
	buffer_load_dwordx4 v[2:5], v35, s[4:7], 0 offen nt
	buffer_load_dwordx4 v[6:9], v35, s[4:7], s20 offen nt
	buffer_load_dwordx4 v[10:13], v35, s[4:7], s21 offen nt
	buffer_load_dwordx4 v[14:17], v35, s[4:7], s22 offen nt
	s_waitcnt vmcnt(4)
	v_max3_f32 v49, v18, v19, v20
	v_max3_f32 v50, v21, v22, v23
	v_max3_f32 v49, v49, v24, v25
	v_max3_f32 v50, v50, v26, v27
	v_max3_f32 v49, v49, v28, v29
	v_max3_f32 v50, v50, v30, v31
	v_max3_f32 v49, v49, v32, v33
	v_max_f32_e32 v49, v49, v50
	v_mov_b32_e32 v50, v49
	s_nop 1
	v_permlane32_swap_b32_e32 v49, v50
	v_max_f32_e32 v49, v49, v50
	v_fmamk_f32 v49, v49, 0x3fb8aa3b, v48
	v_fma_f32 v18, v18, s16, -v49
	v_exp_f32_e32 v18, v18
	v_fma_f32 v19, v19, s16, -v49
	v_exp_f32_e32 v19, v19
	v_fma_f32 v20, v20, s16, -v49
	v_exp_f32_e32 v20, v20
	v_fma_f32 v21, v21, s16, -v49
	v_exp_f32_e32 v21, v21
	v_fma_f32 v22, v22, s16, -v49
	v_exp_f32_e32 v22, v22
	v_fma_f32 v23, v23, s16, -v49
	v_exp_f32_e32 v23, v23
	v_fma_f32 v24, v24, s16, -v49
	v_exp_f32_e32 v24, v24
	v_fma_f32 v25, v25, s16, -v49
	v_exp_f32_e32 v25, v25
	v_fma_f32 v26, v26, s16, -v49
	v_exp_f32_e32 v26, v26
	v_fma_f32 v27, v27, s16, -v49
	v_exp_f32_e32 v27, v27
	v_fma_f32 v28, v28, s16, -v49
	v_exp_f32_e32 v28, v28
	v_fma_f32 v29, v29, s16, -v49
	v_exp_f32_e32 v29, v29
	v_fma_f32 v30, v30, s16, -v49
	v_exp_f32_e32 v30, v30
	v_fma_f32 v31, v31, s16, -v49
	v_exp_f32_e32 v31, v31
	v_fma_f32 v32, v32, s16, -v49
	v_exp_f32_e32 v32, v32
	v_fma_f32 v33, v33, s16, -v49
	v_exp_f32_e32 v33, v33
	v_add_f32_e32 v50, v18, v19
	v_add_f32_e32 v51, v20, v21
	v_add_f32_e32 v50, v50, v22
	v_add_f32_e32 v51, v51, v23
	v_add_f32_e32 v50, v50, v24
	v_add_f32_e32 v51, v51, v25
	v_add_f32_e32 v50, v50, v26
	v_add_f32_e32 v51, v51, v27
	v_add_f32_e32 v50, v50, v28
	v_add_f32_e32 v51, v51, v29
	v_add_f32_e32 v50, v50, v30
	v_add_f32_e32 v51, v51, v31
	v_add_f32_e32 v50, v50, v32
	v_add_f32_e32 v51, v51, v33
	v_add_f32_e32 v50, v50, v51
	v_mov_b32_e32 v51, v50
	s_nop 1
	v_permlane32_swap_b32_e32 v50, v51
	v_add_f32_e32 v50, v50, v51
	v_log_f32_e32 v50, v50
	v_cvt_pk_f16_f32 v52, v18, v19
	v_cvt_pk_f16_f32 v53, v20, v21
	v_cvt_pk_f16_f32 v54, v22, v23
	v_cvt_pk_f16_f32 v55, v24, v25
	v_cvt_pk_f16_f32 v56, v26, v27
	v_cvt_pk_f16_f32 v57, v28, v29
	v_cvt_pk_f16_f32 v58, v30, v31
	v_cvt_pk_f16_f32 v59, v32, v33
	v_add_f32_e32 v50, 0x41600000, v50
	v_mul_f32_e32 v50, 0xbf317218, v50
	v_cndmask_b32_e64 v51, v50, 1.0, vcc
	s_waitcnt vmcnt(3)
	ds_write_b128 v38, v[2:5]
	s_waitcnt vmcnt(2)
	ds_write_b128 v38, v[6:9] offset:1152
	s_waitcnt vmcnt(1)
	ds_write_b128 v38, v[10:13] offset:2304
	s_waitcnt vmcnt(0)
	ds_write_b128 v38, v[14:17] offset:3456
	ds_read_b128 v[60:63], v39
	ds_read_b128 v[64:67], v39 offset:16
	ds_read_b128 v[68:71], v39 offset:32
	ds_read_b128 v[72:75], v39 offset:48
	s_waitcnt lgkmcnt(2)
	v_max3_f32 v76, v60, v61, v62
	v_max3_f32 v77, v63, v64, v65
	v_max_f32_e32 v76, v76, v66
	v_max_f32_e32 v77, v77, v67
	s_waitcnt lgkmcnt(0)
	v_max3_f32 v76, v76, v68, v69
	v_max3_f32 v77, v77, v70, v71
	v_max3_f32 v76, v76, v72, v73
	v_max3_f32 v77, v77, v74, v75
	v_max_f32_e32 v76, v76, v77
	v_mov_b32_e32 v77, v76
	s_nop 1
	v_permlane32_swap_b32_e32 v76, v77
	v_max_f32_e32 v76, v76, v77
	v_cndmask_b32_e32 v78, 1.0, v76, vcc
	v_fmamk_f32 v79, v76, 0x3fb8aa3b, v48
	v_fma_f32 v60, v60, s16, -v79
	v_mfma_f32_32x32x2_f32 v[80:95], v51, v78, 0
	v_exp_f32_e32 v60, v60
	v_fma_f32 v61, v61, s16, -v79
	v_exp_f32_e32 v61, v61
	v_fma_f32 v62, v62, s16, -v79
	v_exp_f32_e32 v62, v62
	v_fma_f32 v63, v63, s16, -v79
	v_exp_f32_e32 v63, v63
	v_fma_f32 v64, v64, s16, -v79
	v_exp_f32_e32 v64, v64
	v_fma_f32 v65, v65, s16, -v79
	v_exp_f32_e32 v65, v65
	v_fma_f32 v66, v66, s16, -v79
	v_exp_f32_e32 v66, v66
	v_fma_f32 v67, v67, s16, -v79
	v_exp_f32_e32 v67, v67
	v_fma_f32 v68, v68, s16, -v79
	v_exp_f32_e32 v68, v68
	v_cvt_pk_f16_f32 v96, v60, v61
	v_cvt_pk_f16_f32 v97, v62, v63
	v_cvt_pk_f16_f32 v98, v64, v65
	v_cvt_pk_f16_f32 v99, v66, v67
	v_fma_f32 v69, v69, s16, -v79
	v_exp_f32_e32 v69, v69
	v_fma_f32 v70, v70, s16, -v79
	v_exp_f32_e32 v70, v70
	v_mfma_f32_32x32x16_f16 v[104:119], v[52:55], v[96:99], 0
	v_fma_f32 v71, v71, s16, -v79
	v_exp_f32_e32 v71, v71
	v_fma_f32 v72, v72, s16, -v79
	v_exp_f32_e32 v72, v72
	v_fma_f32 v73, v73, s16, -v79
	v_exp_f32_e32 v73, v73
	v_fma_f32 v74, v74, s16, -v79
	v_exp_f32_e32 v74, v74
	v_fma_f32 v75, v75, s16, -v79
	v_exp_f32_e32 v75, v75
	v_cvt_pk_f16_f32 v100, v68, v69
	v_cvt_pk_f16_f32 v101, v70, v71
	v_cvt_pk_f16_f32 v102, v72, v73
	v_cvt_pk_f16_f32 v103, v74, v75
	s_nop 1
	v_mfma_f32_32x32x16_f16 v[104:119], v[56:59], v[100:103], v[104:119]
	s_nop 11
	v_log_f32_e32 v104, v104
	v_log_f32_e32 v105, v105
	v_log_f32_e32 v106, v106
	v_log_f32_e32 v107, v107
	v_log_f32_e32 v108, v108
	v_log_f32_e32 v109, v109
	v_log_f32_e32 v110, v110
	v_log_f32_e32 v111, v111
	v_fmac_f32_e32 v80, s17, v104
	v_fmac_f32_e32 v81, s17, v105
	v_fmac_f32_e32 v82, s17, v106
	v_fmac_f32_e32 v83, s17, v107
	global_store_dwordx4 v36, v[80:83], s[8:9]
	v_log_f32_e32 v112, v112
	v_log_f32_e32 v113, v113
	v_log_f32_e32 v114, v114
	v_log_f32_e32 v115, v115
	v_fmac_f32_e32 v84, s17, v108
	v_fmac_f32_e32 v85, s17, v109
	v_fmac_f32_e32 v86, s17, v110
	v_fmac_f32_e32 v87, s17, v111
	global_store_dwordx4 v36, v[84:87], s[8:9] offset:32
	v_log_f32_e32 v116, v116
	v_log_f32_e32 v117, v117
	v_log_f32_e32 v118, v118
	v_log_f32_e32 v119, v119
	v_fmac_f32_e32 v88, s17, v112
	v_fmac_f32_e32 v89, s17, v113
	v_fmac_f32_e32 v90, s17, v114
	v_fmac_f32_e32 v91, s17, v115
	global_store_dwordx4 v36, v[88:91], s[8:9] offset:64
	v_fmac_f32_e32 v92, s17, v116
	v_fmac_f32_e32 v93, s17, v117
	v_fmac_f32_e32 v94, s17, v118
	v_fmac_f32_e32 v95, s17, v119
	global_store_dwordx4 v36, v[92:95], s[8:9] offset:96
	s_endpgm

	.amdhsa_kernel _Z16sum_layer_kernelPKfS0_Pf
		.amdhsa_group_segment_fixed_size 18432
		.amdhsa_private_segment_fixed_size 0
		.amdhsa_kernarg_size 24
		.amdhsa_user_sgpr_count 2
		.amdhsa_user_sgpr_dispatch_ptr 0
		.amdhsa_user_sgpr_queue_ptr 0
		.amdhsa_user_sgpr_kernarg_segment_ptr 1
		.amdhsa_user_sgpr_dispatch_id 0
		.amdhsa_user_sgpr_kernarg_preload_length 0
		.amdhsa_user_sgpr_kernarg_preload_offset 0
		.amdhsa_user_sgpr_private_segment_size 0
		.amdhsa_uses_dynamic_stack 0
		.amdhsa_enable_private_segment 0
		.amdhsa_system_sgpr_workgroup_id_x 1
		.amdhsa_system_sgpr_workgroup_id_y 0
		.amdhsa_system_sgpr_workgroup_id_z 0
		.amdhsa_system_sgpr_workgroup_info 0
		.amdhsa_system_vgpr_workitem_id 0
		.amdhsa_next_free_vgpr 120
		.amdhsa_next_free_sgpr 23
		.amdhsa_accum_offset 120
		.amdhsa_reserve_vcc 1
		.amdhsa_float_round_mode_32 0
		.amdhsa_float_round_mode_16_64 0
		.amdhsa_float_denorm_mode_32 3
		.amdhsa_float_denorm_mode_16_64 3
		.amdhsa_dx10_clamp 1
		.amdhsa_ieee_mode 1
		.amdhsa_fp16_overflow 0
		.amdhsa_tg_split 0
		.amdhsa_exception_fp_ieee_invalid_op 0
		.amdhsa_exception_fp_denorm_src 0
		.amdhsa_exception_fp_ieee_div_zero 0
		.amdhsa_exception_fp_ieee_overflow 0
		.amdhsa_exception_fp_ieee_underflow 0
		.amdhsa_exception_fp_ieee_inexact 0
		.amdhsa_exception_int_div_zero 0
	.end_amdhsa_kernel

amdhsa.kernels:
  - .agpr_count:     0
    .args:
      - .address_space:  global
        .offset:         0
        .size:           8
        .value_kind:     global_buffer
      - .address_space:  global
        .offset:         8
        .size:           8
        .value_kind:     global_buffer
      - .address_space:  global
        .offset:         16
        .size:           8
        .value_kind:     global_buffer
    .group_segment_fixed_size: 18432
    .kernarg_segment_align: 8
    .kernarg_segment_size: 24
    .language:       OpenCL C
    .language_version:
      - 2
      - 0
    .max_flat_workgroup_size: 256
    .name:           _Z16sum_layer_kernelPKfS0_Pf
    .private_segment_fixed_size: 0
    .sgpr_count:     29
    .sgpr_spill_count: 0
    .symbol:         _Z16sum_layer_kernelPKfS0_Pf.kd
    .uniform_work_group_size: 1
    .uses_dynamic_stack: false
    .vgpr_count:     120
    .vgpr_spill_count: 0
    .wavefront_size: 64
